# adds to the MFMA snake order: P2 LOGG via scalar load + counted loop-top wait (no vmcnt(0) in the body), P3 scan loop software-pipelined with exact counted waits
# baseline (speedup 1.0000x reference)
; #define LAS __attribute__((address_space(3)))
; #define GAS __attribute__((address_space(1)))
; #define LAS __attribute__((address_space(3)))
; DI void ret_kv_phase(LAS unsigned char* lds, const bf16* PROJ, float* KVB, const float* ssqsb, float* rsb, int bx, int G, int tid) {
;     const int lane = tid & 63, w = __builtin_amdgcn_readfirstlane(tid >> 6), r = lane & 31, h = lane >> 5;
;     LAS unsigned char* KT = lds + L_KT; LAS unsigned char* VT = lds + L_VT;
;     const int te = w >> 1, td0 = 2 * (w & 1), which = (tid >> 7) & 1;
;     v4u kreg[4], vreg[4]; f32x4 pp = {0.f, 0.f, 0.f, 0.f};
;     if (bx < 2048) { const int n = bx & 63, hd = (bx >> 6) & 15, b = bx >> 10; const size_t m0 = (size_t)b * SEQ + 128 * n;
;         tile_ld(kreg, PROJ + m0 * INW + C_RK + 128 * hd, INW, tid); tile_ld(vreg, PROJ + m0 * INW + C_RV + 128 * hd, INW, tid);
;         pp = *(const GAS f32x4*)(ssqsb + ((m0 + (tid & 127)) * 32 + 16 * which + hd) * 4); }
;     for (int unit = bx; unit < 2048; unit += G) {
.LBB0_396:
	s_cmp_lt_i32 s74, 3
	s_cselect_b64 s[0:1], -1, 0
	s_and_b64 s[4:5], s[0:1], s[4:5]
	s_andn2_b64 vcc, exec, s[4:5]
	s_cbranch_vccnz .LBB0_404
	s_cmpk_gt_i32 s2, 0x7ff
	v_readfirstlane_b32 s0, v0
	s_cbranch_scc1 .LBB0_404
	s_add_u32 s10, s84, 0xe00000
	s_addc_u32 s11, s85, 0
	s_add_u32 s12, s84, 0x600000
	s_addc_u32 s13, s85, 0
	s_ashr_i32 s6, s2, 10
	s_ashr_i32 s7, s6, 31
	s_lshl_b32 s22, s2, 7
	s_lshl_b64 s[6:7], s[6:7], 13
	s_and_b32 s8, s22, 0x1f80
	s_or_b32 s6, s6, s8
	s_mul_i32 s8, s7, 0x7000
	s_mul_hi_u32 s9, s6, 0x7000
	s_and_b32 s14, s0, 64
	s_lshr_b32 s1, s0, 7
	s_bfe_u32 s3, s2, 0x40006
	s_add_i32 s9, s9, s8
	s_mul_i32 s8, s6, 0x7000
	s_add_u32 s8, s42, s8
	s_addc_u32 s9, s43, s9
	s_lshl_b32 s16, s3, 8
	v_lshlrev_b32_e32 v2, 3, v0
	v_and_b32_e32 v2, 0x78, v2
	s_add_u32 s8, s8, s16
	v_or_b32_e32 v12, 0x200, v0
	v_mov_b32_e32 v71, 0
	v_lshlrev_b32_e32 v70, 1, v2
	s_addc_u32 s9, s9, 0
	v_lshrrev_b32_e32 v9, 4, v0
	v_lshrrev_b32_e32 v13, 4, v12
	v_lshl_add_u64 v[4:5], s[8:9], 0, v[70:71]
	s_mov_b64 s[16:17], 0x2000
	v_mul_u32_u24_e32 v8, 0x3800, v9
	v_mul_u32_u24_e32 v12, 0x3800, v13
	v_lshl_add_u64 v[6:7], v[4:5], 0, s[16:17]
	v_lshlrev_b32_e32 v70, 1, v8
	v_lshlrev_b32_e32 v14, 1, v12
	v_mov_b32_e32 v15, v71
	v_lshl_add_u64 v[10:11], v[6:7], 0, v[70:71]
	v_lshl_add_u64 v[16:17], v[6:7], 0, v[14:15]
	global_load_dwordx4 v[34:37], v[10:11], off
	global_load_dwordx4 v[38:41], v[16:17], off
	v_or_b32_e32 v16, 0x600, v0
	v_lshrrev_b32_e32 v17, 4, v16
	s_mov_b32 s23, 0x1c0000
	v_mul_u32_u24_e32 v16, 0x3800, v17
	v_add_co_u32_e32 v10, vcc, s23, v10
	v_lshlrev_b32_e32 v18, 1, v16
	v_mov_b32_e32 v19, v71
	s_mov_b64 s[18:19], 0x3000
	v_addc_co_u32_e32 v11, vcc, 0, v11, vcc
	v_lshl_add_u64 v[6:7], v[6:7], 0, v[18:19]
	v_lshl_add_u64 v[4:5], v[4:5], 0, s[18:19]
	global_load_dwordx4 v[42:45], v[10:11], off
	global_load_dwordx4 v[46:49], v[6:7], off
	v_lshl_add_u64 v[6:7], v[4:5], 0, v[70:71]
	v_lshl_add_u64 v[10:11], v[4:5], 0, v[14:15]
	global_load_dwordx4 v[50:53], v[6:7], off
	global_load_dwordx4 v[54:57], v[10:11], off
	v_add_co_u32_e32 v6, vcc, s23, v6
	v_lshl_add_u64 v[4:5], v[4:5], 0, v[18:19]
	s_nop 0
	v_addc_co_u32_e32 v7, vcc, 0, v7, vcc
	v_and_b32_e32 v72, 0x7f, v0
	global_load_dwordx4 v[58:61], v[6:7], off
	global_load_dwordx4 v[66:69], v[4:5], off
	v_or_b32_e32 v4, s6, v72
	v_mov_b32_e32 v5, s7
	v_lshrrev_b32_e32 v6, 3, v0
	v_lshlrev_b64 v[4:5], 5, v[4:5]
	v_and_b32_e32 v74, 16, v6
	v_or3_b32 v4, v4, s3, v74
	v_lshl_add_u64 v[4:5], v[4:5], 4, s[10:11]
	global_load_dwordx4 v[62:65], v[4:5], off
	v_lshlrev_b32_e32 v4, 4, v0
	v_lshlrev_b32_e32 v7, 2, v0
	v_and_b32_e32 v4, 0xf0, v4
	s_lshl_b32 s8, s1, 5
	v_and_b32_e32 v5, 4, v6
	v_and_b32_e32 v6, 16, v0
	v_and_b32_e32 v7, 12, v7
	v_add_u32_e32 v18, 0, v4
	v_lshrrev_b32_e32 v4, 2, v0
	v_or3_b32 v10, s8, v6, v7
	v_or3_b32 v6, v7, v6, s14
	s_movk_i32 s3, 0x140
	v_and_b32_e32 v76, 0x60, v4
	v_and_or_b32 v4, v4, 3, v5
	v_lshlrev_b32_e32 v73, 1, v6
	v_mov_b32_e32 v6, 0x6400
	v_mad_u32_u24 v22, v4, s3, v6
	v_mov_b32_e32 v6, 0x7800
	v_mad_u32_u24 v23, v4, s3, v6
	v_mov_b32_e32 v6, 0x8c00
	v_and_b32_e32 v3, 31, v0
	s_lshl_b32 s8, s1, 12
	v_mul_u32_u24_e32 v20, 0x140, v4
	v_mad_u32_u24 v75, v4, s3, 0
	v_mad_u32_u24 v24, v4, s3, v6
	v_lshlrev_b32_e32 v4, 6, v0
	v_and_b32_e32 v25, 0x800, v4
	v_or_b32_e32 v4, s8, v3
	v_lshlrev_b32_e32 v11, 7, v5
	s_lshl_b32 s0, s0, 2
	v_ashrrev_i32_e32 v5, 31, v4
	s_ashr_i32 s3, s2, 31
	s_and_b32 s0, s0, 0x100
	v_lshlrev_b64 v[6:7], 2, v[4:5]
	s_lshl_b64 s[20:21], s[2:3], 16
	v_or3_b32 v6, v25, s0, v6
	s_or_b32 s3, s8, s14
	v_lshl_add_u64 v[78:79], s[84:85], 0, v[6:7]
	v_or_b32_e32 v6, s3, v3
	v_or3_b32 v4, v11, s14, v4
	v_lshl_add_u32 v19, v10, 1, 0
	v_or_b32_e32 v10, v6, v11
	v_lshl_add_u64 v[4:5], v[4:5], 2, s[84:85]
	s_mov_b64 s[26:27], 0x42e00080
	v_lshl_add_u64 v[84:85], v[4:5], 0, s[26:27]
	v_or_b32_e32 v4, 0xc80, v10
	v_ashrrev_i32_e32 v5, 31, v4
	s_mov_b64 s[8:9], 0x42e00000
	v_lshl_add_u64 v[4:5], v[4:5], 2, s[84:85]
	v_ashrrev_i32_e32 v7, 31, v6
	v_lshl_add_u64 v[86:87], v[4:5], 0, s[8:9]
	v_lshlrev_b64 v[4:5], 2, v[6:7]
	v_or_b32_e32 v4, v4, v25
	v_lshl_add_u64 v[4:5], s[84:85], 0, v[4:5]
	s_mov_b64 s[26:27], 0x42e00400
	v_lshl_add_u64 v[88:89], v[4:5], 0, s[26:27]
	v_or_b32_e32 v4, 0xc00, v10
	v_ashrrev_i32_e32 v5, 31, v4
	v_lshl_add_u64 v[4:5], v[4:5], 2, s[84:85]
	v_ashrrev_i32_e32 v11, 31, v10
	v_lshl_add_u64 v[90:91], v[4:5], 0, s[8:9]
	v_lshl_add_u64 v[4:5], v[10:11], 2, s[84:85]
	v_lshl_add_u64 v[92:93], v[4:5], 0, s[8:9]
	v_or_b32_e32 v4, 0x400, v10
	v_ashrrev_i32_e32 v5, 31, v4
	v_lshl_add_u64 v[4:5], v[4:5], 2, s[84:85]
	v_lshl_add_u64 v[94:95], v[4:5], 0, s[8:9]
	v_or_b32_e32 v4, 0x480, v10
	v_ashrrev_i32_e32 v5, 31, v4
	v_lshl_add_u64 v[4:5], v[4:5], 2, s[84:85]
	v_lshl_add_u64 v[96:97], v[4:5], 0, s[8:9]
	v_or_b32_e32 v4, 0x500, v10
	v_ashrrev_i32_e32 v5, 31, v4
	v_lshl_add_u64 v[4:5], v[4:5], 2, s[84:85]
	v_lshl_add_u64 v[98:99], v[4:5], 0, s[8:9]
	v_or_b32_e32 v4, 0x580, v10
	v_ashrrev_i32_e32 v5, 31, v4
	v_lshl_add_u64 v[4:5], v[4:5], 2, s[84:85]
	v_lshl_add_u64 v[100:101], v[4:5], 0, s[8:9]
	v_or_b32_e32 v4, 0x800, v10
	v_ashrrev_i32_e32 v5, 31, v4
	v_lshl_add_u64 v[4:5], v[4:5], 2, s[84:85]
	v_lshl_add_u64 v[102:103], v[4:5], 0, s[8:9]
	v_or_b32_e32 v4, 0x880, v10
	v_ashrrev_i32_e32 v5, 31, v4
	v_lshl_add_u64 v[4:5], v[4:5], 2, s[84:85]
	v_or_b32_e32 v14, 0xd80, v10
	v_lshl_add_u64 v[104:105], v[4:5], 0, s[8:9]
	v_or_b32_e32 v4, 0x900, v10
	v_ashrrev_i32_e32 v15, 31, v14
	v_ashrrev_i32_e32 v5, 31, v4
	v_lshl_add_u64 v[14:15], v[14:15], 2, s[84:85]
	v_lshl_add_u64 v[4:5], v[4:5], 2, s[84:85]
	v_lshl_add_u64 v[80:81], v[14:15], 0, s[8:9]
	v_or_b32_e32 v14, 0xd00, v10
	v_lshl_add_u64 v[106:107], v[4:5], 0, s[8:9]
	v_or_b32_e32 v4, 0x980, v10
	v_ashrrev_i32_e32 v15, 31, v14
	v_ashrrev_i32_e32 v5, 31, v4
	v_mul_u32_u24_e32 v9, 0x140, v9
	v_mul_u32_u24_e32 v13, 0x140, v13
	v_mul_u32_u24_e32 v17, 0x140, v17
	s_movk_i32 s6, 0xff
	v_or_b32_e32 v21, 64, v73
	s_ashr_i32 s81, s80, 31
	v_lshl_add_u64 v[14:15], v[14:15], 2, s[84:85]
	v_lshl_add_u64 v[4:5], v[4:5], 2, s[84:85]
	s_mov_b32 s15, 0
	v_cmp_lt_u32_e64 s[6:7], s6, v0
	v_mov_b32_e32 v77, v71
	s_lshl_b32 s24, s80, 7
	s_lshl_b64 s[0:1], s[80:81], 16
	v_lshl_add_u64 v[82:83], v[14:15], 0, s[8:9]
	v_lshl_add_u64 v[108:109], v[4:5], 0, s[8:9]
	v_add_u32_e32 v118, v18, v9
	v_add_u32_e32 v119, v18, v13
	v_add_u32_e32 v120, v18, v17
	v_mov_b32_e32 v121, 0x358637bd
	s_mov_b32 s3, 0x800000
	v_lshlrev_b32_e32 v70, 1, v2
	v_lshlrev_b32_e32 v110, 1, v8
	v_lshlrev_b32_e32 v112, 1, v12
	v_lshlrev_b32_e32 v114, 1, v16
	v_add_u32_e32 v122, v19, v20
	v_add_u32_e32 v123, v75, v21
	v_add_u32_e32 v124, v19, v22
	v_add_u32_e32 v125, v19, v23
	v_add_u32_e32 v126, v19, v24
	s_mov_b32 s25, 0x42e00000
	s_mov_b32 s26, 0x42e01000
	s_mov_b32 s27, 0x42e02000
	s_mov_b32 s28, 0x42e03000
	s_mov_b32 s29, s2
	s_waitcnt vmcnt(0)
	s_branch .LBB0_400
; #define GAS __attribute__((address_space(1)))
; #define MFMA32(a, b, c) __builtin_amdgcn_mfma_f32_32x32x16_bf16((a), (b), (c), 0, 0, 0)
; DI void ret_kv_phase(LAS unsigned char* lds, const bf16* PROJ, float* KVB, const float* ssqsb, float* rsb, int bx, int G, int tid) {
;     ...
;         { const int u2 = unit + G < 2048 ? unit + G : unit, n2 = u2 & 63, hd2 = (u2 >> 6) & 15, b2 = u2 >> 10; const size_t m2 = (size_t)b2 * SEQ + 128 * n2;
;           tile_ld(kreg, PROJ + m2 * INW + C_RK + 128 * hd2, INW, tid); tile_ld(vreg, PROJ + m2 * INW + C_RV + 128 * hd2, INW, tid);
;           pp = *(const GAS f32x4*)(ssqsb + ((m2 + (tid & 127)) * 32 + 16 * which + hd2) * 4); }
;         asm volatile("" ::: "memory");
;         f32x16 acc[2];
; #pragma unroll
;         for (int t = 0; t < 2; ++t)
; #pragma unroll
;             for (int i = 0; i < 16; ++i) acc[t][i] = 0.f;
; #pragma unroll
;         for (int ks = 0; ks < 8; ++ks) {
;             const bf16x8 a = tr_frag(VT, VSTR, 16 * ks, 32 * te, lane);
; #pragma unroll
;             for (int t = 0; t < 2; ++t) { const bf16x8 bb = tr_frag(KT, VSTR, 16 * ks, 32 * (td0 + t), lane); acc[t] = MFMA32(a, bb, acc[t]); }
;         }
;         const float sc = __expf(127.0f * LOGG[hd]);
.LBB0_399:
	s_or_b64 exec, exec, s[8:9]
	s_bfe_u32 s99, s29, 0x40006
	s_lshl_b32 s99, s99, 2
	s_getpc_b64 s[100:101]
	s_add_u32 s100, s100, _ZN3pg84LOGGE@rel32@lo+4
	s_addc_u32 s101, s101, _ZN3pg84LOGGE@rel32@hi+12
	s_load_dword s98, s[100:101], s99
	s_add_i32 s14, s29, s80
	s_cmpk_lt_i32 s14, 0x800
	s_cselect_b64 s[8:9], -1, 0
	s_and_b64 vcc, s[8:9], exec
	s_cselect_b32 s29, s14, s29
	s_ashr_i32 s8, s29, 10
	s_ashr_i32 s9, s8, 31
	s_lshl_b64 s[30:31], s[8:9], 13
	s_lshl_b32 s8, s29, 7
	s_and_b32 s8, s8, 0x1f80
	s_bfe_u32 s33, s29, 0x40006
	s_or_b32 s29, s30, s8
	s_mul_i32 s8, s31, 0x7000
	s_mul_hi_u32 s9, s29, 0x7000
	s_add_i32 s9, s9, s8
	s_mul_i32 s8, s29, 0x7000
	s_add_u32 s8, s42, s8
	s_addc_u32 s9, s43, s9
	s_lshl_b32 s30, s33, 8
	s_add_u32 s8, s8, s30
	s_addc_u32 s9, s9, 0
	v_lshl_add_u64 v[2:3], s[8:9], 0, v[70:71]
	v_lshl_add_u64 v[4:5], v[2:3], 0, s[16:17]
	v_mov_b32_e32 v111, v71
	v_lshl_add_u64 v[6:7], v[4:5], 0, v[110:111]
	v_mov_b32_e32 v113, v71
	s_waitcnt lgkmcnt(0)
	s_barrier
	v_lshl_add_u64 v[8:9], v[4:5], 0, v[112:113]
	global_load_dwordx4 v[34:37], v[6:7], off
	global_load_dwordx4 v[38:41], v[8:9], off
	v_add_co_u32_e64 v6, s[8:9], s23, v6
	v_mov_b32_e32 v115, v71
	s_nop 0
	v_addc_co_u32_e64 v7, s[8:9], 0, v7, s[8:9]
	v_lshl_add_u64 v[4:5], v[4:5], 0, v[114:115]
	v_lshl_add_u64 v[2:3], v[2:3], 0, s[18:19]
	global_load_dwordx4 v[42:45], v[6:7], off
	global_load_dwordx4 v[46:49], v[4:5], off
	v_lshl_add_u64 v[4:5], v[2:3], 0, v[110:111]
	v_lshl_add_u64 v[6:7], v[2:3], 0, v[112:113]
	global_load_dwordx4 v[50:53], v[4:5], off
	global_load_dwordx4 v[54:57], v[6:7], off
	v_add_co_u32_e64 v4, s[8:9], s23, v4
	v_lshl_add_u64 v[2:3], v[2:3], 0, v[114:115]
	s_nop 0
	v_addc_co_u32_e64 v5, s[8:9], 0, v5, s[8:9]
	global_load_dwordx4 v[58:61], v[4:5], off
	global_load_dwordx4 v[66:69], v[2:3], off
	v_mov_b32_e32 v3, s31
	v_or_b32_e32 v2, s29, v72
	v_lshlrev_b64 v[2:3], 5, v[2:3]
	v_or_b32_e32 v2, s33, v2
	v_or_b32_e32 v2, v2, v74
	v_lshl_add_u64 v[2:3], v[2:3], 4, s[10:11]
	global_load_dwordx4 v[62:65], v[2:3], off
	ds_read_b64_tr_b16 v[2:3], v122 offset:40960
	ds_read_b64_tr_b16 v[4:5], v122 offset:43520
	v_add_u32_e32 v111, v75, v73
	ds_read_b64_tr_b16 v[6:7], v111
	ds_read_b64_tr_b16 v[8:9], v111 offset:2560
	ds_read_b64_tr_b16 v[128:129], v122 offset:46080
	ds_read_b64_tr_b16 v[130:131], v122 offset:48640
	ds_read_b64_tr_b16 v[132:133], v111 offset:5120
	ds_read_b64_tr_b16 v[136:137], v111 offset:38400
	s_waitcnt lgkmcnt(4)
	v_mfma_f32_32x32x16_bf16 v[18:33], v[2:5], v[6:9], 0
	ds_read_b64_tr_b16 v[6:7], v123
	ds_read_b64_tr_b16 v[8:9], v123 offset:2560
	ds_read_b64_tr_b16 v[138:139], v123 offset:5120
	ds_read_b64_tr_b16 v[142:143], v123 offset:38400
	ds_read_b64_tr_b16 v[134:135], v111 offset:7680
	ds_read_b64_tr_b16 v[144:145], v111 offset:10240
	ds_read_b64_tr_b16 v[146:147], v111 offset:12800
	ds_read_b64_tr_b16 v[148:149], v111 offset:15360
	s_add_i32 s22, s22, s24
	s_mov_b32 s29, s14
	s_waitcnt lgkmcnt(6)
	v_mfma_f32_32x32x16_bf16 v[2:17], v[2:5], v[6:9], 0
	s_waitcnt lgkmcnt(3)
	v_mfma_f32_32x32x16_bf16 v[18:33], v[128:131], v[132:135], v[18:33]
	ds_read_b64_tr_b16 v[140:141], v123 offset:7680
	ds_read_b64_tr_b16 v[132:133], v123 offset:10240
	ds_read_b64_tr_b16 v[134:135], v123 offset:12800
	ds_read_b64_tr_b16 v[152:153], v123 offset:15360
	s_waitcnt lgkmcnt(3)
	v_mfma_f32_32x32x16_bf16 v[2:17], v[128:131], v[138:141], v[2:17]
	ds_read_b64_tr_b16 v[128:129], v122 offset:51200
	ds_read_b64_tr_b16 v[130:131], v122 offset:53760
	ds_read_b64_tr_b16 v[138:139], v122 offset:56320
	ds_read_b64_tr_b16 v[140:141], v122 offset:58880
	s_waitcnt lgkmcnt(2)
	v_mfma_f32_32x32x16_bf16 v[18:33], v[128:131], v[144:147], v[18:33]
	v_mfma_f32_32x32x16_bf16 v[2:17], v[128:131], v[132:135], v[2:17]
	ds_read_b64_tr_b16 v[150:151], v111 offset:17920
	ds_read_b64_tr_b16 v[128:129], v111 offset:20480
	ds_read_b64_tr_b16 v[130:131], v111 offset:23040
	ds_read_b64_tr_b16 v[144:145], v111 offset:25600
	s_waitcnt lgkmcnt(3)
	v_mfma_f32_32x32x16_bf16 v[18:33], v[138:141], v[148:151], v[18:33]
	ds_read_b64_tr_b16 v[154:155], v123 offset:17920
	ds_read_b64_tr_b16 v[146:147], v123 offset:20480
	ds_read_b64_tr_b16 v[148:149], v123 offset:23040
	ds_read_b64_tr_b16 v[150:151], v123 offset:25600
	s_waitcnt lgkmcnt(3)
	v_mfma_f32_32x32x16_bf16 v[2:17], v[138:141], v[152:155], v[2:17]
	ds_read_b64_tr_b16 v[138:139], v122 offset:61440
	ds_read_b64_tr_b16 v[140:141], v122 offset:64000
	ds_read_b64_tr_b16 v[132:133], v111 offset:33280
	ds_read_b64_tr_b16 v[134:135], v111 offset:35840
	s_waitcnt lgkmcnt(2)
	v_mfma_f32_32x32x16_bf16 v[18:33], v[138:141], v[128:131], v[18:33]
	v_mfma_f32_32x32x16_bf16 v[2:17], v[138:141], v[146:149], v[2:17]
	ds_read_b64_tr_b16 v[154:155], v124 offset:40960
	ds_read_b64_tr_b16 v[156:157], v124 offset:43520
	ds_read_b64_tr_b16 v[146:147], v111 offset:28160
	ds_read_b64_tr_b16 v[158:159], v123 offset:30720
	ds_read_b64_tr_b16 v[130:131], v111 offset:30720
	ds_read_b64_tr_b16 v[160:161], v123 offset:33280
	ds_read_b64_tr_b16 v[140:141], v123 offset:35840
	ds_read_b64_tr_b16 v[152:153], v123 offset:28160
	v_lshl_add_u64 v[116:117], v[92:93], 0, s[20:21]
	v_lshl_add_u64 v[92:93], v[92:93], 0, s[0:1]
	s_waitcnt lgkmcnt(5)
	v_mfma_f32_32x32x16_bf16 v[18:33], v[154:157], v[144:147], v[18:33]
	s_waitcnt lgkmcnt(0)
	v_mfma_f32_32x32x16_bf16 v[2:17], v[154:157], v[150:153], v[2:17]
	ds_read_b64_tr_b16 v[144:145], v125 offset:40960
	ds_read_b64_tr_b16 v[146:147], v125 offset:43520
	ds_read_b64_tr_b16 v[148:149], v126 offset:40960
	ds_read_b64_tr_b16 v[150:151], v126 offset:43520
	v_mov_b32_e32 v111, s98
	v_mul_f32_e32 v111, 0x42fe0000, v111
	s_waitcnt lgkmcnt(2)
; __device__ __forceinline__ float hsum4(const f32x4 v) { return (v[0] + v[1]) + (v[2] + v[3]); }
; DI int crow(int i, int h) { return (i & 3) + 8 * (i >> 2) + 4 * h; }
; DI void ret_kv_phase(LAS unsigned char* lds, const bf16* PROJ, float* KVB, const float* ssqsb, float* rsb, int bx, int G, int tid) {
;     ...
;     for (int unit = bx; unit < 2048; unit += G) {
;         const int n = unit & 63, hd = (unit >> 6) & 15, b = unit >> 10;
;         __syncthreads();
;         tile_st(KT, VSTR, kreg, tid); tile_st(VT, VSTR, vreg, tid);
;         if (tid < 256) rsb[((size_t)which * 32 + b * 16 + hd) * SEQ + 128 * n + (tid & 127)] = rsqrtf(hsum4(pp) * (1.0f / 128.0f) + EPSN);
;         __syncthreads();
;     ...
;         const float sc = __expf(127.0f * LOGG[hd]);
;         float* o = KVB + (size_t)unit * 16384;
; #pragma unroll
;         for (int t = 0; t < 2; ++t)
; #pragma unroll
;             for (int i = 0; i < 16; ++i) o[(32 * te + crow(i, h)) * 128 + 32 * (td0 + t) + r] = acc[t][i] * sc;
	v_mfma_f32_32x32x16_bf16 v[18:33], v[144:147], v[130:133], v[18:33]
	v_mul_f32_e32 v111, 0x3fb8aa3b, v111
	v_exp_f32_e32 v111, v111
	s_waitcnt lgkmcnt(0)
	v_mfma_f32_32x32x16_bf16 v[18:33], v[148:151], v[134:137], v[18:33]
	v_mfma_f32_32x32x16_bf16 v[2:17], v[144:147], v[158:161], v[2:17]
	s_nop 10
	v_mul_f32_e32 v18, v18, v111
	global_store_dword v[116:117], v18, off
	v_mul_f32_e32 v113, v19, v111
	v_lshl_add_u64 v[18:19], v[88:89], 0, s[20:21]
	v_mul_f32_e32 v20, v20, v111
	global_store_dword v[18:19], v20, off
	v_mul_f32_e32 v20, v21, v111
	global_store_dword v[18:19], v113, off offset:-512
	global_store_dword v[18:19], v20, off offset:512
	v_mul_f32_e32 v20, v22, v111
	v_lshl_add_u64 v[18:19], v[94:95], 0, s[20:21]
	global_store_dword v[18:19], v20, off
	v_mul_f32_e32 v20, v23, v111
	v_lshl_add_u64 v[18:19], v[96:97], 0, s[20:21]
	global_store_dword v[18:19], v20, off
	v_mul_f32_e32 v20, v24, v111
	v_lshl_add_u64 v[18:19], v[98:99], 0, s[20:21]
	global_store_dword v[18:19], v20, off
	v_mul_f32_e32 v20, v25, v111
	v_lshl_add_u64 v[18:19], v[100:101], 0, s[20:21]
	v_mfma_f32_32x32x16_bf16 v[2:17], v[148:151], v[140:143], v[2:17]
	global_store_dword v[18:19], v20, off
	v_mul_f32_e32 v20, v26, v111
	v_lshl_add_u64 v[18:19], v[102:103], 0, s[20:21]
	global_store_dword v[18:19], v20, off
	v_mul_f32_e32 v20, v27, v111
	v_lshl_add_u64 v[18:19], v[104:105], 0, s[20:21]
	global_store_dword v[18:19], v20, off
	v_mul_f32_e32 v20, v28, v111
	v_lshl_add_u64 v[18:19], v[106:107], 0, s[20:21]
	global_store_dword v[18:19], v20, off
	v_mul_f32_e32 v20, v29, v111
	v_lshl_add_u64 v[18:19], v[108:109], 0, s[20:21]
	global_store_dword v[18:19], v20, off
	v_mul_f32_e32 v20, v30, v111
	v_lshl_add_u64 v[18:19], v[90:91], 0, s[20:21]
	global_store_dword v[18:19], v20, off
	v_mul_f32_e32 v20, v31, v111
	v_lshl_add_u64 v[18:19], v[86:87], 0, s[20:21]
	global_store_dword v[18:19], v20, off
	v_mul_f32_e32 v20, v32, v111
	v_lshl_add_u64 v[18:19], v[82:83], 0, s[20:21]
	global_store_dword v[18:19], v20, off
	v_mul_f32_e32 v20, v33, v111
	v_lshl_add_u64 v[18:19], v[80:81], 0, s[20:21]
	global_store_dword v[18:19], v20, off
	v_mul_f32_e32 v2, v2, v111
	v_lshl_add_u64 v[18:19], v[84:85], 0, s[20:21]
	global_store_dword v[18:19], v2, off
	v_mul_f32_e32 v20, v3, v111
	v_lshl_add_u64 v[2:3], v[78:79], 0, s[20:21]
	v_add_co_u32_e64 v18, s[8:9], s25, v2
	v_mul_f32_e32 v4, v4, v111
	s_nop 0
	v_addc_co_u32_e64 v19, s[8:9], 0, v3, s[8:9]
	global_store_dword v[18:19], v4, off offset:1152
	v_mul_f32_e32 v4, v5, v111
	global_store_dword v[18:19], v4, off offset:1664
	v_add_co_u32_e64 v4, s[8:9], s26, v2
	v_mul_f32_e32 v6, v6, v111
	s_nop 0
	v_addc_co_u32_e64 v5, s[8:9], 0, v3, s[8:9]
	global_store_dword v[4:5], v6, off offset:128
	v_mul_f32_e32 v6, v7, v111
	global_store_dword v[4:5], v6, off offset:640
	v_mul_f32_e32 v6, v8, v111
	global_store_dword v[4:5], v6, off offset:1152
	v_mul_f32_e32 v6, v9, v111
	global_store_dword v[4:5], v6, off offset:1664
	v_add_co_u32_e64 v4, s[8:9], s27, v2
	v_mul_f32_e32 v6, v10, v111
	s_nop 0
	v_addc_co_u32_e64 v5, s[8:9], 0, v3, s[8:9]
	global_store_dword v[4:5], v6, off offset:128
	v_mul_f32_e32 v6, v11, v111
	global_store_dword v[4:5], v6, off offset:640
	v_mul_f32_e32 v6, v12, v111
	global_store_dword v[4:5], v6, off offset:1152
	v_mul_f32_e32 v6, v13, v111
	v_add_co_u32_e64 v2, s[8:9], s28, v2
	global_store_dword v[4:5], v6, off offset:1664
	v_mul_f32_e32 v4, v14, v111
	v_addc_co_u32_e64 v3, s[8:9], 0, v3, s[8:9]
	global_store_dword v[2:3], v4, off offset:128
	v_mul_f32_e32 v4, v15, v111
	global_store_dword v[2:3], v4, off offset:640
	v_mul_f32_e32 v4, v16, v111
	global_store_dword v[2:3], v4, off offset:1152
	v_mul_f32_e32 v4, v17, v111
	v_lshl_add_u64 v[78:79], v[78:79], 0, s[0:1]
	v_lshl_add_u64 v[80:81], v[80:81], 0, s[0:1]
	v_lshl_add_u64 v[82:83], v[82:83], 0, s[0:1]
	v_lshl_add_u64 v[84:85], v[84:85], 0, s[0:1]
	v_lshl_add_u64 v[86:87], v[86:87], 0, s[0:1]
	v_lshl_add_u64 v[88:89], v[88:89], 0, s[0:1]
	v_lshl_add_u64 v[90:91], v[90:91], 0, s[0:1]
	v_lshl_add_u64 v[94:95], v[94:95], 0, s[0:1]
	v_lshl_add_u64 v[96:97], v[96:97], 0, s[0:1]
	v_lshl_add_u64 v[98:99], v[98:99], 0, s[0:1]
	v_lshl_add_u64 v[100:101], v[100:101], 0, s[0:1]
	v_lshl_add_u64 v[102:103], v[102:103], 0, s[0:1]
	v_lshl_add_u64 v[104:105], v[104:105], 0, s[0:1]
	v_lshl_add_u64 v[106:107], v[106:107], 0, s[0:1]
	v_lshl_add_u64 v[108:109], v[108:109], 0, s[0:1]
	global_store_dword v[18:19], v20, off offset:640
	global_store_dword v[2:3], v4, off offset:1664
	s_cbranch_vccz .LBB0_404
.LBB0_400:
	s_bfe_u32 s14, s29, 0x40006
	v_mov_b64_e32 v[116:117], s[14:15]
	s_waitcnt vmcnt(32) lgkmcnt(0)
	s_barrier
	ds_write_b128 v118, v[34:37]
	ds_write_b128 v119, v[38:41]
	ds_write_b128 v118, v[42:45] offset:20480
	ds_write_b128 v120, v[46:49]
	ds_write_b128 v118, v[50:53] offset:40960
	ds_write_b128 v119, v[54:57] offset:40960
	ds_write_b128 v118, v[58:61] offset:61440
	ds_write_b128 v120, v[66:69] offset:40960
	s_and_saveexec_b64 s[8:9], s[6:7]
	s_xor_b64 s[8:9], exec, s[8:9]
	v_mov_b64_e32 v[116:117], s[14:15]
	s_andn2_saveexec_b64 s[8:9], s[8:9]
	s_cbranch_execz .LBB0_399
	v_mov_b32_e32 v2, v63
	v_mov_b32_e32 v3, v64
	v_mov_b32_e32 v63, v65
	v_pk_add_f32 v[2:3], v[2:3], v[62:63]
	s_ashr_i32 s30, s29, 6
	v_add_f32_e32 v2, v2, v3
	v_fmamk_f32 v2, v2, 0x3c000000, v121
	v_mul_f32_e32 v3, 0x4b800000, v2
	v_cmp_gt_f32_e32 vcc, s3, v2
	s_and_b32 s30, s30, -16
	s_ashr_i32 s31, s30, 31
	v_cndmask_b32_e32 v2, v2, v3, vcc
	v_rsq_f32_e32 v2, v2
	v_lshlrev_b32_e32 v4, 2, v72
	v_mov_b32_e32 v5, v71
	v_mul_f32_e32 v3, 0x45800000, v2
	v_cndmask_b32_e32 v6, v2, v3, vcc
	v_lshl_add_u64 v[2:3], s[30:31], 0, v[76:77]
	v_or_b32_e32 v2, s14, v2
	s_and_b32 s14, s22, 0x1f80
	v_lshlrev_b64 v[2:3], 15, v[2:3]
	v_lshl_add_u64 v[2:3], s[12:13], 0, v[2:3]
	s_lshl_b32 s14, s14, 2
	v_lshl_add_u64 v[2:3], v[2:3], 0, s[14:15]
	v_lshl_add_u64 v[2:3], v[2:3], 0, v[4:5]
	global_store_dword v[2:3], v6, off
	s_branch .LBB0_399

; __device__ __forceinline__ unsigned pk_bf16(float lo, float hi) { const f32x2 f = {lo, hi}; const bf16v2 r = __builtin_convertvector(f, bf16v2); return __builtin_bit_cast(unsigned, r); }
; #define GAS __attribute__((address_space(1)))
; DI void ret_scan(const float* __restrict__ KVB, bf16* __restrict__ ST, int gt, int NT) {
;     for (int idx = gt; idx < 32 * 4096; idx += NT) {
;         const int bh = idx >> 12, e4 = idx & 4095; const float dec = __expf(128.0f * LOGG[bh & 15]);
;         f32x4 S = {0.f, 0.f, 0.f, 0.f};
;         for (int n0 = 0; n0 < 64; n0 += 8) {
;             f32x4 kv[8];
; #pragma unroll
;             for (int i = 0; i < 8; ++i) kv[i] = *(const GAS f32x4*)(KVB + ((size_t)(bh * 64 + n0 + i) * 4096 + e4) * 4);
;             asm volatile("" ::: "memory");
; #pragma unroll
;             for (int i = 0; i < 8; ++i) { v2u w; w.x = pk_bf16(S[0], S[1]); w.y = pk_bf16(S[2], S[3]); *(GAS v2u*)(ST + ((size_t)(bh * 64 + n0 + i) * 4096 + e4) * 4) = w; S = S * dec + kv[i]; }
;         }
.LBB0_458:
	s_cmp_lt_i32 s74, 4
	s_cselect_b64 s[0:1], -1, 0
	s_and_b64 s[0:1], s[0:1], s[6:7]
	s_andn2_b64 vcc, exec, s[0:1]
	v_add_u32_e32 v208, s73, v0
	s_cbranch_vccnz .LBB0_465
	s_mov_b32 s3, 0x20000
	v_cmp_gt_i32_e32 vcc, s3, v208
	s_and_saveexec_b64 s[4:5], vcc
	s_cbranch_execz .LBB0_464
	s_add_u32 s100, s84, 0x42e00000
	s_addc_u32 s101, s85, 0
	s_add_u32 s98, s84, 0x4ae00000
	s_addc_u32 s99, s85, 0
	v_lshlrev_b32_e32 v2, 2, v0
	v_lshl_or_b32 v14, s2, 11, v2
	s_lshl_b32 s3, s80, 11
	s_mov_b64 s[6:7], 0
	s_movk_i32 s12, 0x7ff8
	s_mov_b32 s13, 0xfff0
	s_mov_b32 s14, 0x4ae00000
	s_mov_b32 s15, 0x4ae08000
	s_mov_b32 s16, 0x4ae10000
	s_mov_b32 s17, 0x4ae18000
	s_mov_b32 s18, 0x4ae20000
	s_mov_b32 s19, 0x4ae28000
	s_mov_b32 s20, 0x4ae30000
	s_mov_b32 s21, 0x4ae38000
	s_mov_b64 s[8:9], 0x40000
	s_mov_b64 s[10:11], 0x80000
	s_mov_b32 s22, 0x1ffff
	v_mov_b32_e32 v15, v208
	s_getpc_b64 s[24:25]
	s_add_u32 s24, s24, _ZN3pg84LOGGE@rel32@lo+4
	s_addc_u32 s25, s25, _ZN3pg84LOGGE@rel32@hi+12
.LBB0_461:
	v_ashrrev_i32_e32 v2, 12, v15
	v_lshlrev_b32_e32 v3, 2, v2
	v_and_b32_e32 v3, 60, v3
	global_load_dword v4, v3, s[24:25]
	v_lshlrev_b32_e32 v6, 6, v2
	v_ashrrev_i32_e32 v7, 31, v6
	v_lshlrev_b32_e32 v5, 1, v14
	v_lshlrev_b32_e32 v8, 2, v14
	v_mov_b32_e32 v10, 0
	v_lshlrev_b64 v[2:3], 15, v[6:7]
	v_lshlrev_b64 v[6:7], 16, v[6:7]
	s_mov_b32 s23, -8
	v_mov_b32_e32 v11, v10
	v_mov_b32_e32 v12, v10
	v_and_or_b32 v2, v5, s12, v2
	v_and_or_b32 v6, v8, s13, v6
	v_mov_b32_e32 v13, v10
	s_waitcnt vmcnt(0)
	v_mul_f32_e32 v4, 0x43000000, v4
	v_mul_f32_e32 v4, 0x3fb8aa3b, v4
	v_exp_f32_e32 v4, v4
	s_nop 0
	v_mov_b32_e32 v5, v4
	v_mov_b32_e32 v8, v4
	v_mov_b32_e32 v9, v4
	global_load_dwordx4 v[16:19], v6, s[100:101]
	v_add_u32_e32 v51, 0x10000, v6
	global_load_dwordx4 v[20:23], v51, s[100:101]
	v_add_u32_e32 v51, 0x20000, v6
	global_load_dwordx4 v[24:27], v51, s[100:101]
	v_add_u32_e32 v51, 0x30000, v6
	global_load_dwordx4 v[28:31], v51, s[100:101]
	v_add_u32_e32 v51, 0x40000, v6
	global_load_dwordx4 v[32:35], v51, s[100:101]
	v_add_u32_e32 v51, 0x50000, v6
	global_load_dwordx4 v[36:39], v51, s[100:101]
	v_add_u32_e32 v51, 0x60000, v6
	global_load_dwordx4 v[40:43], v51, s[100:101]
	v_add_u32_e32 v51, 0x70000, v6
	global_load_dwordx4 v[44:47], v51, s[100:101]
	v_add_u32_e32 v6, 0x80000, v6
	global_load_dwordx4 v[62:65], v6, s[100:101]
	v_add_u32_e32 v51, 0x10000, v6
	global_load_dwordx4 v[66:69], v51, s[100:101]
	v_add_u32_e32 v51, 0x20000, v6
	global_load_dwordx4 v[70:73], v51, s[100:101]
	v_add_u32_e32 v51, 0x30000, v6
	global_load_dwordx4 v[74:77], v51, s[100:101]
	v_add_u32_e32 v51, 0x40000, v6
	global_load_dwordx4 v[78:81], v51, s[100:101]
	v_add_u32_e32 v51, 0x50000, v6
	global_load_dwordx4 v[82:85], v51, s[100:101]
	v_add_u32_e32 v51, 0x60000, v6
	global_load_dwordx4 v[86:89], v51, s[100:101]
	v_add_u32_e32 v51, 0x70000, v6
	global_load_dwordx4 v[90:93], v51, s[100:101]
	v_add_u32_e32 v6, 0x80000, v6
	s_waitcnt vmcnt(8)
	v_cvt_pk_bf16_f32 v48, v10, v11
	v_cvt_pk_bf16_f32 v49, v12, v13
	global_store_dwordx2 v2, v[48:49], s[98:99]
	v_pk_fma_f32 v[12:13], v[8:9], v[12:13], v[18:19]
	v_pk_fma_f32 v[10:11], v[4:5], v[10:11], v[16:17]
	v_cvt_pk_bf16_f32 v52, v10, v11
	v_cvt_pk_bf16_f32 v53, v12, v13
	v_add_u32_e32 v50, 0x8000, v2
	global_store_dwordx2 v50, v[52:53], s[98:99]
	v_pk_fma_f32 v[12:13], v[8:9], v[12:13], v[22:23]
	v_pk_fma_f32 v[10:11], v[4:5], v[10:11], v[20:21]
	v_cvt_pk_bf16_f32 v48, v10, v11
	v_cvt_pk_bf16_f32 v49, v12, v13
	v_add_u32_e32 v50, 0x10000, v2
	global_store_dwordx2 v50, v[48:49], s[98:99]
	v_pk_fma_f32 v[12:13], v[8:9], v[12:13], v[26:27]
	v_pk_fma_f32 v[10:11], v[4:5], v[10:11], v[24:25]
	v_cvt_pk_bf16_f32 v52, v10, v11
	v_cvt_pk_bf16_f32 v53, v12, v13
	v_add_u32_e32 v50, 0x18000, v2
	global_store_dwordx2 v50, v[52:53], s[98:99]
	v_pk_fma_f32 v[12:13], v[8:9], v[12:13], v[30:31]
	v_pk_fma_f32 v[10:11], v[4:5], v[10:11], v[28:29]
	v_cvt_pk_bf16_f32 v48, v10, v11
	v_cvt_pk_bf16_f32 v49, v12, v13
	v_add_u32_e32 v50, 0x20000, v2
	global_store_dwordx2 v50, v[48:49], s[98:99]
	v_pk_fma_f32 v[12:13], v[8:9], v[12:13], v[34:35]
	v_pk_fma_f32 v[10:11], v[4:5], v[10:11], v[32:33]
	v_cvt_pk_bf16_f32 v52, v10, v11
	v_cvt_pk_bf16_f32 v53, v12, v13
	v_add_u32_e32 v50, 0x28000, v2
	global_store_dwordx2 v50, v[52:53], s[98:99]
	v_pk_fma_f32 v[12:13], v[8:9], v[12:13], v[38:39]
	v_pk_fma_f32 v[10:11], v[4:5], v[10:11], v[36:37]
	v_cvt_pk_bf16_f32 v48, v10, v11
	v_cvt_pk_bf16_f32 v49, v12, v13
	v_add_u32_e32 v50, 0x30000, v2
	global_store_dwordx2 v50, v[48:49], s[98:99]
	v_pk_fma_f32 v[12:13], v[8:9], v[12:13], v[42:43]
	v_pk_fma_f32 v[10:11], v[4:5], v[10:11], v[40:41]
	v_cvt_pk_bf16_f32 v52, v10, v11
	v_cvt_pk_bf16_f32 v53, v12, v13
	v_add_u32_e32 v50, 0x38000, v2
	global_store_dwordx2 v50, v[52:53], s[98:99]
	v_pk_fma_f32 v[12:13], v[8:9], v[12:13], v[46:47]
	v_pk_fma_f32 v[10:11], v[4:5], v[10:11], v[44:45]
	v_add_u32_e32 v2, 0x40000, v2
	s_mov_b32 s23, 3
; __device__ __forceinline__ unsigned pk_bf16(float lo, float hi) { const f32x2 f = {lo, hi}; const bf16v2 r = __builtin_convertvector(f, bf16v2); return __builtin_bit_cast(unsigned, r); }
; #define GAS __attribute__((address_space(1)))
; DI void ret_scan(const float* __restrict__ KVB, bf16* __restrict__ ST, int gt, int NT) {
;     ...
;         for (int n0 = 0; n0 < 64; n0 += 8) {
;             f32x4 kv[8];
; #pragma unroll
;             for (int i = 0; i < 8; ++i) kv[i] = *(const GAS f32x4*)(KVB + ((size_t)(bh * 64 + n0 + i) * 4096 + e4) * 4);
;             asm volatile("" ::: "memory");
; #pragma unroll
;             for (int i = 0; i < 8; ++i) { v2u w; w.x = pk_bf16(S[0], S[1]); w.y = pk_bf16(S[2], S[3]); *(GAS v2u*)(ST + ((size_t)(bh * 64 + n0 + i) * 4096 + e4) * 4) = w; S = S * dec + kv[i]; }
;         }
.Lp3_loop:
	global_load_dwordx4 v[16:19], v6, s[100:101]
	v_add_u32_e32 v51, 0x10000, v6
	global_load_dwordx4 v[20:23], v51, s[100:101]
	v_add_u32_e32 v51, 0x20000, v6
	global_load_dwordx4 v[24:27], v51, s[100:101]
	v_add_u32_e32 v51, 0x30000, v6
	global_load_dwordx4 v[28:31], v51, s[100:101]
	v_add_u32_e32 v51, 0x40000, v6
	global_load_dwordx4 v[32:35], v51, s[100:101]
	v_add_u32_e32 v51, 0x50000, v6
	global_load_dwordx4 v[36:39], v51, s[100:101]
	v_add_u32_e32 v51, 0x60000, v6
	global_load_dwordx4 v[40:43], v51, s[100:101]
	v_add_u32_e32 v51, 0x70000, v6
	global_load_dwordx4 v[44:47], v51, s[100:101]
	v_add_u32_e32 v6, 0x80000, v6
	s_waitcnt vmcnt(16)
	v_cvt_pk_bf16_f32 v48, v10, v11
	v_cvt_pk_bf16_f32 v49, v12, v13
	global_store_dwordx2 v2, v[48:49], s[98:99]
	v_pk_fma_f32 v[12:13], v[8:9], v[12:13], v[64:65]
	v_pk_fma_f32 v[10:11], v[4:5], v[10:11], v[62:63]
	v_cvt_pk_bf16_f32 v52, v10, v11
	v_cvt_pk_bf16_f32 v53, v12, v13
	v_add_u32_e32 v50, 0x8000, v2
	global_store_dwordx2 v50, v[52:53], s[98:99]
	v_pk_fma_f32 v[12:13], v[8:9], v[12:13], v[68:69]
	v_pk_fma_f32 v[10:11], v[4:5], v[10:11], v[66:67]
	v_cvt_pk_bf16_f32 v48, v10, v11
	v_cvt_pk_bf16_f32 v49, v12, v13
	v_add_u32_e32 v50, 0x10000, v2
	global_store_dwordx2 v50, v[48:49], s[98:99]
	v_pk_fma_f32 v[12:13], v[8:9], v[12:13], v[72:73]
	v_pk_fma_f32 v[10:11], v[4:5], v[10:11], v[70:71]
	v_cvt_pk_bf16_f32 v52, v10, v11
	v_cvt_pk_bf16_f32 v53, v12, v13
	v_add_u32_e32 v50, 0x18000, v2
	global_store_dwordx2 v50, v[52:53], s[98:99]
	v_pk_fma_f32 v[12:13], v[8:9], v[12:13], v[76:77]
	v_pk_fma_f32 v[10:11], v[4:5], v[10:11], v[74:75]
	v_cvt_pk_bf16_f32 v48, v10, v11
	v_cvt_pk_bf16_f32 v49, v12, v13
	v_add_u32_e32 v50, 0x20000, v2
	global_store_dwordx2 v50, v[48:49], s[98:99]
	v_pk_fma_f32 v[12:13], v[8:9], v[12:13], v[80:81]
	v_pk_fma_f32 v[10:11], v[4:5], v[10:11], v[78:79]
	v_cvt_pk_bf16_f32 v52, v10, v11
	v_cvt_pk_bf16_f32 v53, v12, v13
	v_add_u32_e32 v50, 0x28000, v2
	global_store_dwordx2 v50, v[52:53], s[98:99]
	v_pk_fma_f32 v[12:13], v[8:9], v[12:13], v[84:85]
	v_pk_fma_f32 v[10:11], v[4:5], v[10:11], v[82:83]
	v_cvt_pk_bf16_f32 v48, v10, v11
	v_cvt_pk_bf16_f32 v49, v12, v13
	v_add_u32_e32 v50, 0x30000, v2
	global_store_dwordx2 v50, v[48:49], s[98:99]
	v_pk_fma_f32 v[12:13], v[8:9], v[12:13], v[88:89]
	v_pk_fma_f32 v[10:11], v[4:5], v[10:11], v[86:87]
	v_cvt_pk_bf16_f32 v52, v10, v11
	v_cvt_pk_bf16_f32 v53, v12, v13
	v_add_u32_e32 v50, 0x38000, v2
	global_store_dwordx2 v50, v[52:53], s[98:99]
	v_pk_fma_f32 v[12:13], v[8:9], v[12:13], v[92:93]
	v_pk_fma_f32 v[10:11], v[4:5], v[10:11], v[90:91]
	v_add_u32_e32 v2, 0x40000, v2
	global_load_dwordx4 v[62:65], v6, s[100:101]
	v_add_u32_e32 v51, 0x10000, v6
	global_load_dwordx4 v[66:69], v51, s[100:101]
	v_add_u32_e32 v51, 0x20000, v6
	global_load_dwordx4 v[70:73], v51, s[100:101]
	v_add_u32_e32 v51, 0x30000, v6
	global_load_dwordx4 v[74:77], v51, s[100:101]
	v_add_u32_e32 v51, 0x40000, v6
	global_load_dwordx4 v[78:81], v51, s[100:101]
	v_add_u32_e32 v51, 0x50000, v6
	global_load_dwordx4 v[82:85], v51, s[100:101]
	v_add_u32_e32 v51, 0x60000, v6
	global_load_dwordx4 v[86:89], v51, s[100:101]
	v_add_u32_e32 v51, 0x70000, v6
	global_load_dwordx4 v[90:93], v51, s[100:101]
	v_add_u32_e32 v6, 0x80000, v6
	s_waitcnt vmcnt(16)
	v_cvt_pk_bf16_f32 v48, v10, v11
	v_cvt_pk_bf16_f32 v49, v12, v13
	global_store_dwordx2 v2, v[48:49], s[98:99]
	v_pk_fma_f32 v[12:13], v[8:9], v[12:13], v[18:19]
	v_pk_fma_f32 v[10:11], v[4:5], v[10:11], v[16:17]
	v_cvt_pk_bf16_f32 v52, v10, v11
	v_cvt_pk_bf16_f32 v53, v12, v13
	v_add_u32_e32 v50, 0x8000, v2
	global_store_dwordx2 v50, v[52:53], s[98:99]
	v_pk_fma_f32 v[12:13], v[8:9], v[12:13], v[22:23]
	v_pk_fma_f32 v[10:11], v[4:5], v[10:11], v[20:21]
	v_cvt_pk_bf16_f32 v48, v10, v11
	v_cvt_pk_bf16_f32 v49, v12, v13
	v_add_u32_e32 v50, 0x10000, v2
	global_store_dwordx2 v50, v[48:49], s[98:99]
	v_pk_fma_f32 v[12:13], v[8:9], v[12:13], v[26:27]
	v_pk_fma_f32 v[10:11], v[4:5], v[10:11], v[24:25]
	v_cvt_pk_bf16_f32 v52, v10, v11
	v_cvt_pk_bf16_f32 v53, v12, v13
	v_add_u32_e32 v50, 0x18000, v2
	global_store_dwordx2 v50, v[52:53], s[98:99]
	v_pk_fma_f32 v[12:13], v[8:9], v[12:13], v[30:31]
	v_pk_fma_f32 v[10:11], v[4:5], v[10:11], v[28:29]
	v_cvt_pk_bf16_f32 v48, v10, v11
	v_cvt_pk_bf16_f32 v49, v12, v13
	v_add_u32_e32 v50, 0x20000, v2
	global_store_dwordx2 v50, v[48:49], s[98:99]
	v_pk_fma_f32 v[12:13], v[8:9], v[12:13], v[34:35]
	v_pk_fma_f32 v[10:11], v[4:5], v[10:11], v[32:33]
	v_cvt_pk_bf16_f32 v52, v10, v11
	v_cvt_pk_bf16_f32 v53, v12, v13
	v_add_u32_e32 v50, 0x28000, v2
	global_store_dwordx2 v50, v[52:53], s[98:99]
	v_pk_fma_f32 v[12:13], v[8:9], v[12:13], v[38:39]
	v_pk_fma_f32 v[10:11], v[4:5], v[10:11], v[36:37]
	v_cvt_pk_bf16_f32 v48, v10, v11
	v_cvt_pk_bf16_f32 v49, v12, v13
	v_add_u32_e32 v50, 0x30000, v2
	global_store_dwordx2 v50, v[48:49], s[98:99]
	v_pk_fma_f32 v[12:13], v[8:9], v[12:13], v[42:43]
	v_pk_fma_f32 v[10:11], v[4:5], v[10:11], v[40:41]
	v_cvt_pk_bf16_f32 v52, v10, v11
	v_cvt_pk_bf16_f32 v53, v12, v13
	v_add_u32_e32 v50, 0x38000, v2
	global_store_dwordx2 v50, v[52:53], s[98:99]
	v_pk_fma_f32 v[12:13], v[8:9], v[12:13], v[46:47]
	v_pk_fma_f32 v[10:11], v[4:5], v[10:11], v[44:45]
	v_add_u32_e32 v2, 0x40000, v2
	s_sub_u32 s23, s23, 1
	s_cmp_lg_u32 s23, 0
	s_cbranch_scc1 .Lp3_loop
; __device__ __forceinline__ unsigned pk_bf16(float lo, float hi) { const f32x2 f = {lo, hi}; const bf16v2 r = __builtin_convertvector(f, bf16v2); return __builtin_bit_cast(unsigned, r); }
; #define GAS __attribute__((address_space(1)))
; DI void ret_scan(const float* __restrict__ KVB, bf16* __restrict__ ST, int gt, int NT) {
;     for (int idx = gt; idx < 32 * 4096; idx += NT) {
;         const int bh = idx >> 12, e4 = idx & 4095; const float dec = __expf(128.0f * LOGG[bh & 15]);
;         f32x4 S = {0.f, 0.f, 0.f, 0.f};
;         for (int n0 = 0; n0 < 64; n0 += 8) {
;             f32x4 kv[8];
; #pragma unroll
;             for (int i = 0; i < 8; ++i) kv[i] = *(const GAS f32x4*)(KVB + ((size_t)(bh * 64 + n0 + i) * 4096 + e4) * 4);
;             asm volatile("" ::: "memory");
; #pragma unroll
;             for (int i = 0; i < 8; ++i) { v2u w; w.x = pk_bf16(S[0], S[1]); w.y = pk_bf16(S[2], S[3]); *(GAS v2u*)(ST + ((size_t)(bh * 64 + n0 + i) * 4096 + e4) * 4) = w; S = S * dec + kv[i]; }
;         }
	s_waitcnt vmcnt(8)
	v_cvt_pk_bf16_f32 v48, v10, v11
	v_cvt_pk_bf16_f32 v49, v12, v13
	global_store_dwordx2 v2, v[48:49], s[98:99]
	v_pk_fma_f32 v[12:13], v[8:9], v[12:13], v[64:65]
	v_pk_fma_f32 v[10:11], v[4:5], v[10:11], v[62:63]
	v_cvt_pk_bf16_f32 v52, v10, v11
	v_cvt_pk_bf16_f32 v53, v12, v13
	v_add_u32_e32 v50, 0x8000, v2
	global_store_dwordx2 v50, v[52:53], s[98:99]
	v_pk_fma_f32 v[12:13], v[8:9], v[12:13], v[68:69]
	v_pk_fma_f32 v[10:11], v[4:5], v[10:11], v[66:67]
	v_cvt_pk_bf16_f32 v48, v10, v11
	v_cvt_pk_bf16_f32 v49, v12, v13
	v_add_u32_e32 v50, 0x10000, v2
	global_store_dwordx2 v50, v[48:49], s[98:99]
	v_pk_fma_f32 v[12:13], v[8:9], v[12:13], v[72:73]
	v_pk_fma_f32 v[10:11], v[4:5], v[10:11], v[70:71]
	v_cvt_pk_bf16_f32 v52, v10, v11
	v_cvt_pk_bf16_f32 v53, v12, v13
	v_add_u32_e32 v50, 0x18000, v2
	global_store_dwordx2 v50, v[52:53], s[98:99]
	v_pk_fma_f32 v[12:13], v[8:9], v[12:13], v[76:77]
	v_pk_fma_f32 v[10:11], v[4:5], v[10:11], v[74:75]
	v_cvt_pk_bf16_f32 v48, v10, v11
	v_cvt_pk_bf16_f32 v49, v12, v13
	v_add_u32_e32 v50, 0x20000, v2
	global_store_dwordx2 v50, v[48:49], s[98:99]
	v_pk_fma_f32 v[12:13], v[8:9], v[12:13], v[80:81]
	v_pk_fma_f32 v[10:11], v[4:5], v[10:11], v[78:79]
	v_cvt_pk_bf16_f32 v52, v10, v11
	v_cvt_pk_bf16_f32 v53, v12, v13
	v_add_u32_e32 v50, 0x28000, v2
	global_store_dwordx2 v50, v[52:53], s[98:99]
	v_pk_fma_f32 v[12:13], v[8:9], v[12:13], v[84:85]
	v_pk_fma_f32 v[10:11], v[4:5], v[10:11], v[82:83]
	v_cvt_pk_bf16_f32 v48, v10, v11
	v_cvt_pk_bf16_f32 v49, v12, v13
	v_add_u32_e32 v50, 0x30000, v2
	global_store_dwordx2 v50, v[48:49], s[98:99]
	v_pk_fma_f32 v[12:13], v[8:9], v[12:13], v[88:89]
	v_pk_fma_f32 v[10:11], v[4:5], v[10:11], v[86:87]
	v_cvt_pk_bf16_f32 v52, v10, v11
	v_cvt_pk_bf16_f32 v53, v12, v13
	v_add_u32_e32 v50, 0x38000, v2
	global_store_dwordx2 v50, v[52:53], s[98:99]
	v_pk_fma_f32 v[12:13], v[8:9], v[12:13], v[92:93]
	v_pk_fma_f32 v[10:11], v[4:5], v[10:11], v[90:91]
	v_add_u32_e32 v2, 0x40000, v2
	v_add_u32_e32 v15, s72, v15
	v_cmp_lt_i32_e32 vcc, s22, v15
	s_or_b64 s[6:7], vcc, s[6:7]
	v_add_u32_e32 v14, s3, v14
	s_andn2_b64 exec, exec, s[6:7]
	s_cbranch_execnz .LBB0_461

; __global__ void __launch_bounds__(NWAVES * 64, 2) mk_fwd(Args args) {
	.amdhsa_kernel _Z6mk_fwd4Args
		.amdhsa_group_segment_fixed_size 0
		.amdhsa_private_segment_fixed_size 0
		.amdhsa_kernarg_size 448
		.amdhsa_user_sgpr_count 2
		.amdhsa_user_sgpr_dispatch_ptr 0
		.amdhsa_user_sgpr_queue_ptr 0
		.amdhsa_user_sgpr_kernarg_segment_ptr 1
		.amdhsa_user_sgpr_dispatch_id 0
		.amdhsa_user_sgpr_kernarg_preload_length 0
		.amdhsa_user_sgpr_kernarg_preload_offset 0
		.amdhsa_user_sgpr_private_segment_size 0
		.amdhsa_uses_dynamic_stack 0
		.amdhsa_enable_private_segment 0
		.amdhsa_system_sgpr_workgroup_id_x 1
		.amdhsa_system_sgpr_workgroup_id_y 0
		.amdhsa_system_sgpr_workgroup_id_z 0
		.amdhsa_system_sgpr_workgroup_info 0
		.amdhsa_system_vgpr_workitem_id 0
		.amdhsa_next_free_vgpr 255
		.amdhsa_next_free_sgpr 102
		.amdhsa_accum_offset 256
		.amdhsa_reserve_vcc 1
		.amdhsa_float_round_mode_32 0
		.amdhsa_float_round_mode_16_64 0
		.amdhsa_float_denorm_mode_32 3
		.amdhsa_float_denorm_mode_16_64 3
		.amdhsa_dx10_clamp 1
		.amdhsa_ieee_mode 1
		.amdhsa_fp16_overflow 0
		.amdhsa_tg_split 0
		.amdhsa_exception_fp_ieee_invalid_op 0
		.amdhsa_exception_fp_denorm_src 0
		.amdhsa_exception_fp_ieee_div_zero 0
		.amdhsa_exception_fp_ieee_overflow 0
		.amdhsa_exception_fp_ieee_underflow 0
		.amdhsa_exception_fp_ieee_inexact 0
		.amdhsa_exception_int_div_zero 0
	.end_amdhsa_kernel

; __global__ void __launch_bounds__(NWAVES * 64, 2) mk_fwd(Args args) {
amdhsa.kernels:
  - .agpr_count:     0
    .args:
      - .offset:         0
        .size:           192
        .value_kind:     by_value
      - .offset:         192
        .size:           4
        .value_kind:     hidden_block_count_x
      - .offset:         196
        .size:           4
        .value_kind:     hidden_block_count_y
      - .offset:         200
        .size:           4
        .value_kind:     hidden_block_count_z
      - .offset:         204
        .size:           2
        .value_kind:     hidden_group_size_x
      - .offset:         206
        .size:           2
        .value_kind:     hidden_group_size_y
      - .offset:         208
        .size:           2
        .value_kind:     hidden_group_size_z
      - .offset:         210
        .size:           2
        .value_kind:     hidden_remainder_x
      - .offset:         212
        .size:           2
        .value_kind:     hidden_remainder_y
      - .offset:         214
        .size:           2
        .value_kind:     hidden_remainder_z
      - .offset:         232
        .size:           8
        .value_kind:     hidden_global_offset_x
      - .offset:         240
        .size:           8
        .value_kind:     hidden_global_offset_y
      - .offset:         248
        .size:           8
        .value_kind:     hidden_global_offset_z
      - .offset:         256
        .size:           2
        .value_kind:     hidden_grid_dims
      - .offset:         312
        .size:           4
        .value_kind:     hidden_dynamic_lds_size
    .group_segment_fixed_size: 0
    .kernarg_segment_align: 8
    .kernarg_segment_size: 448
    .language:       OpenCL C
    .language_version:
      - 2
      - 0
    .max_flat_workgroup_size: 512
    .name:           _Z6mk_fwd4Args
    .private_segment_fixed_size: 0
    .sgpr_count:     108
    .sgpr_spill_count: 34
    .symbol:         _Z6mk_fwd4Args.kd
    .uniform_work_group_size: 1
    .uses_dynamic_stack: false
    .vgpr_count:     255
    .vgpr_spill_count: 0
    .wavefront_size: 64
